# baseline (speedup 1.0000x reference)
_Z11gemm_kernelPKfPKDF16bS0_Pf:
	s_load_dwordx8 s[4:11], s[0:1], 0x0
	s_and_b32 s16, s2, 7
	s_lshr_b32 s17, s2, 3
	s_lshr_b32 s18, s16, 2
	s_lshl_b32 s19, s16, 6
	s_add_u32 s19, s19, s17
	s_and_b32 s20, s19, 3
	v_lshrrev_b32_e32 v7, 6, v0
	v_lshrrev_b32_e32 v1, 4, v0
	v_lshlrev_b32_e32 v1, 9, v1
	v_readfirstlane_b32 s21, v7
	v_and_b32_e32 v8, 15, v0
	v_lshl_or_b32 v1, v8, 4, v1
	v_lshlrev_b32_e32 v2, 12, v7
	v_and_b32_e32 v9, 63, v0
	v_lshl_or_b32 v2, v9, 4, v2
	v_bfe_u32 v3, v0, 4, 4
	v_lshlrev_b32_e32 v3, 6, v3
	v_and_b32_e32 v9, 7, v0
	v_lshl_or_b32 v3, v9, 3, v3
	v_bfe_u32 v9, v0, 7, 1
	v_lshlrev_b32_e32 v9, 5, v9
	v_xor_b32_e32 v3, v3, v9
	v_lshrrev_b32_e32 v9, 8, v0
	v_lshlrev_b32_e32 v9, 1, v9
	v_bfe_u32 v10, v0, 3, 1
	v_or_b32_e32 v9, v9, v10
	v_lshl_or_b32 v3, v9, 10, v3
	v_lshlrev_b32_e32 v10, 6, v10
	v_xor_b32_e32 v3, v3, v10
	v_lshlrev_b32_e32 v9, 6, v8
	v_bfe_u32 v10, v0, 4, 2
	v_lshl_or_b32 v9, v10, 4, v9
	v_bfe_u32 v11, v0, 3, 1
	v_lshlrev_b32_e32 v11, 5, v11
	v_xor_b32_e32 v9, v9, v11
	v_lshrrev_b32_e32 v11, 8, v0
	v_lshl_or_b32 v4, v11, 14, v9
	v_xor_b32_e32 v252, 64, v4
	v_and_b32_e32 v12, 3, v7
	v_lshl_or_b32 v5, v12, 13, v9
	v_add_u32_e32 v5, 0x10000, v5
	v_lshl_or_b32 v13, v11, 7, v8
	v_lshlrev_b32_e32 v13, 9, v13
	v_and_b32_e32 v14, 1, v7
	v_lshl_or_b32 v13, v14, 8, v13
	v_lshl_or_b32 v248, v10, 4, v13
	v_lshlrev_b32_e32 v249, 4, v10
	s_and_b32 s46, s21, 3
	s_lshr_b32 s47, s46, 1
	s_lshl_b32 s40, s20, 1
	s_add_u32 s47, s47, s40
	s_lshl_b32 s47, s47, 1
	s_add_u32 s47, s47, s18
	s_lshl_b32 s47, s47, 23
	s_lshr_b32 s40, s19, 2
	s_and_b32 s40, s40, 63
	s_lshl_b32 s40, s40, 17
	s_lshl_b32 s41, s18, 23
	s_or_b32 s22, s40, s41
	s_add_u32 s36, s47, s40
	s_add_u32 s42, s19, 32
	s_lshr_b32 s42, s42, 2
	s_and_b32 s42, s42, 63
	s_lshl_b32 s42, s42, 17
	s_or_b32 s23, s42, s41
	s_add_u32 s37, s47, s42
	s_lshl_b32 s40, s18, 2
	s_add_u32 s40, s40, s20
	s_lshl_b32 s24, s40, 19
	s_lshl_b32 s27, s21, 12
	s_add_u32 s27, s27, 0x10000
	s_add_u32 s32, s27, 0x18000
	s_waitcnt lgkmcnt(0)
	s_mov_b32 s12, s6
	s_and_b32 s13, s7, 0xffff
	s_mov_b32 s14, 0x7fffffff
	s_mov_b32 s15, 0x20000
	s_and_b32 s5, s5, 0xffff
	s_mov_b32 s6, 0x7fffffff
	s_mov_b32 s7, 0x20000
	s_mov_b32 s28, s10
	s_and_b32 s29, s11, 0xffff
	s_mov_b32 s30, 0x7fffffff
	s_mov_b32 s31, 0x20000
	s_lshl_b32 s40, s18, 12
	s_lshl_b32 s41, s20, 10
	s_add_u32 s40, s40, s41
	s_lshl_b32 s41, s46, 8
	s_add_u32 s40, s40, s41
	s_add_u32 s34, s8, s40
	s_addc_u32 s35, s9, 0
	global_load_dwordx4 v[120:123], v249, s[34:35] offset:0
	global_load_dwordx4 v[124:127], v249, s[34:35] offset:64
	global_load_dwordx4 v[128:131], v249, s[34:35] offset:128
	global_load_dwordx4 v[132:135], v249, s[34:35] offset:192
	s_mov_b32 s41, s22
	buffer_load_dwordx4 v[8:11], v1, s[4:7], s41 offen sc0 nt
	s_add_u32 s42, s41, 0x4000
	buffer_load_dwordx4 v[12:15], v1, s[4:7], s42 offen sc0 nt
	s_add_u32 s42, s41, 0x8000
	buffer_load_dwordx4 v[16:19], v1, s[4:7], s42 offen sc0 nt
	s_add_u32 s42, s41, 0xc000
	buffer_load_dwordx4 v[20:23], v1, s[4:7], s42 offen sc0 nt
	s_add_u32 s42, s41, 0x10000
	buffer_load_dwordx4 v[24:27], v1, s[4:7], s42 offen sc0 nt
	s_add_u32 s42, s41, 0x14000
	buffer_load_dwordx4 v[28:31], v1, s[4:7], s42 offen sc0 nt
	s_add_u32 s42, s41, 0x18000
	buffer_load_dwordx4 v[32:35], v1, s[4:7], s42 offen sc0 nt
	s_add_u32 s42, s41, 0x1c000
	buffer_load_dwordx4 v[36:39], v1, s[4:7], s42 offen sc0 nt
	s_mov_b32 m0, s27
	s_mov_b32 s44, s24
	buffer_load_dwordx4 v2, s[12:15], s44 offen sc1 lds
	buffer_load_dwordx4 v2, s[12:15], s44 offen offset:1024 sc1 lds
	buffer_load_dwordx4 v2, s[12:15], s44 offen offset:2048 sc1 lds
	buffer_load_dwordx4 v2, s[12:15], s44 offen offset:3072 sc1 lds
	s_or_b32 s41, s22, 0x100
	buffer_load_dwordx4 v[40:43], v1, s[4:7], s41 offen sc0 nt
	s_add_u32 s42, s41, 0x4000
	buffer_load_dwordx4 v[44:47], v1, s[4:7], s42 offen sc0 nt
	s_add_u32 s42, s41, 0x8000
	buffer_load_dwordx4 v[48:51], v1, s[4:7], s42 offen sc0 nt
	s_add_u32 s42, s41, 0xc000
	buffer_load_dwordx4 v[52:55], v1, s[4:7], s42 offen sc0 nt
	s_add_u32 s42, s41, 0x10000
	buffer_load_dwordx4 v[56:59], v1, s[4:7], s42 offen sc0 nt
	s_add_u32 s42, s41, 0x14000
	buffer_load_dwordx4 v[60:63], v1, s[4:7], s42 offen sc0 nt
	s_add_u32 s42, s41, 0x18000
	buffer_load_dwordx4 v[64:67], v1, s[4:7], s42 offen sc0 nt
	s_add_u32 s42, s41, 0x1c000
	buffer_load_dwordx4 v[68:71], v1, s[4:7], s42 offen sc0 nt
	s_add_u32 s40, s27, 0x8000
	s_mov_b32 m0, s40
	s_add_u32 s44, s24, 0x8000
	buffer_load_dwordx4 v2, s[12:15], s44 offen sc1 lds
	buffer_load_dwordx4 v2, s[12:15], s44 offen offset:1024 sc1 lds
	buffer_load_dwordx4 v2, s[12:15], s44 offen offset:2048 sc1 lds
	buffer_load_dwordx4 v2, s[12:15], s44 offen offset:3072 sc1 lds
	s_add_u32 s26, s27, 0x10000
	s_mov_b32 s33, 0
	s_mov_b32 s25, 3
	s_mov_b32 s39, 0
	s_waitcnt vmcnt(24)
	v_mov_b32_e32 v136, v120
	v_mov_b32_e32 v137, v121
	v_mov_b32_e32 v138, v122
	v_mov_b32_e32 v139, v123
	v_mov_b32_e32 v140, v124
	v_mov_b32_e32 v141, v125
	v_mov_b32_e32 v142, v126
	v_mov_b32_e32 v143, v127
	v_mov_b32_e32 v144, v128
	v_mov_b32_e32 v145, v129
	v_mov_b32_e32 v146, v130
	v_mov_b32_e32 v147, v131
	v_mov_b32_e32 v148, v132
	v_mov_b32_e32 v149, v133
	v_mov_b32_e32 v150, v134
	v_mov_b32_e32 v151, v135
	v_mov_b32_e32 v152, v120
	v_mov_b32_e32 v153, v121
	v_mov_b32_e32 v154, v122
	v_mov_b32_e32 v155, v123
	v_mov_b32_e32 v156, v124
	v_mov_b32_e32 v157, v125
	v_mov_b32_e32 v158, v126
	v_mov_b32_e32 v159, v127
	v_mov_b32_e32 v160, v128
	v_mov_b32_e32 v161, v129
	v_mov_b32_e32 v162, v130
	v_mov_b32_e32 v163, v131
	v_mov_b32_e32 v164, v132
	v_mov_b32_e32 v165, v133
	v_mov_b32_e32 v166, v134
	v_mov_b32_e32 v167, v135
	v_mov_b32_e32 v168, v120
	v_mov_b32_e32 v169, v121
	v_mov_b32_e32 v170, v122
	v_mov_b32_e32 v171, v123
	v_mov_b32_e32 v172, v124
	v_mov_b32_e32 v173, v125
	v_mov_b32_e32 v174, v126
	v_mov_b32_e32 v175, v127
	v_mov_b32_e32 v176, v128
	v_mov_b32_e32 v177, v129
	v_mov_b32_e32 v178, v130
	v_mov_b32_e32 v179, v131
	v_mov_b32_e32 v180, v132
	v_mov_b32_e32 v181, v133
	v_mov_b32_e32 v182, v134
	v_mov_b32_e32 v183, v135
	v_mov_b32_e32 v184, v120
	v_mov_b32_e32 v185, v121
	v_mov_b32_e32 v186, v122
	v_mov_b32_e32 v187, v123
	v_mov_b32_e32 v188, v124
	v_mov_b32_e32 v189, v125
	v_mov_b32_e32 v190, v126
	v_mov_b32_e32 v191, v127
	v_mov_b32_e32 v192, v128
	v_mov_b32_e32 v193, v129
	v_mov_b32_e32 v194, v130
	v_mov_b32_e32 v195, v131
	v_mov_b32_e32 v196, v132
	v_mov_b32_e32 v197, v133
	v_mov_b32_e32 v198, v134
	v_mov_b32_e32 v199, v135
	v_mov_b32_e32 v200, v120
	v_mov_b32_e32 v201, v121
	v_mov_b32_e32 v202, v122
	v_mov_b32_e32 v203, v123
	v_mov_b32_e32 v204, v124
	v_mov_b32_e32 v205, v125
	v_mov_b32_e32 v206, v126
	v_mov_b32_e32 v207, v127
	v_mov_b32_e32 v208, v128
	v_mov_b32_e32 v209, v129
	v_mov_b32_e32 v210, v130
	v_mov_b32_e32 v211, v131
	v_mov_b32_e32 v212, v132
	v_mov_b32_e32 v213, v133
	v_mov_b32_e32 v214, v134
	v_mov_b32_e32 v215, v135
	v_mov_b32_e32 v216, v120
	v_mov_b32_e32 v217, v121
	v_mov_b32_e32 v218, v122
	v_mov_b32_e32 v219, v123
	v_mov_b32_e32 v220, v124
	v_mov_b32_e32 v221, v125
	v_mov_b32_e32 v222, v126
	v_mov_b32_e32 v223, v127
	v_mov_b32_e32 v224, v128
	v_mov_b32_e32 v225, v129
	v_mov_b32_e32 v226, v130
	v_mov_b32_e32 v227, v131
	v_mov_b32_e32 v228, v132
	v_mov_b32_e32 v229, v133
	v_mov_b32_e32 v230, v134
	v_mov_b32_e32 v231, v135
	v_mov_b32_e32 v232, v120
	v_mov_b32_e32 v233, v121
	v_mov_b32_e32 v234, v122
	v_mov_b32_e32 v235, v123
	v_mov_b32_e32 v236, v124
	v_mov_b32_e32 v237, v125
	v_mov_b32_e32 v238, v126
	v_mov_b32_e32 v239, v127
	v_mov_b32_e32 v240, v128
	v_mov_b32_e32 v241, v129
	v_mov_b32_e32 v242, v130
	v_mov_b32_e32 v243, v131
	v_mov_b32_e32 v244, v132
	v_mov_b32_e32 v245, v133
	v_mov_b32_e32 v246, v134
	v_mov_b32_e32 v247, v135
	s_waitcnt vmcnt(22)
	v_cvt_pk_bf16_f32 v8, v8, v9
	v_cvt_pk_bf16_f32 v9, v10, v11
	v_cvt_pk_bf16_f32 v12, v12, v13
	v_cvt_pk_bf16_f32 v13, v14, v15
	ds_write2st64_b64 v3, v[8:9], v[12:13] offset0:0 offset1:8
	s_waitcnt vmcnt(20)
	v_cvt_pk_bf16_f32 v16, v16, v17
	v_cvt_pk_bf16_f32 v17, v18, v19
	v_cvt_pk_bf16_f32 v20, v20, v21
	v_cvt_pk_bf16_f32 v21, v22, v23
	ds_write2st64_b64 v3, v[16:17], v[20:21] offset0:16 offset1:24
	s_waitcnt vmcnt(18)
	v_cvt_pk_bf16_f32 v24, v24, v25
	v_cvt_pk_bf16_f32 v25, v26, v27
	v_cvt_pk_bf16_f32 v28, v28, v29
	v_cvt_pk_bf16_f32 v29, v30, v31
	ds_write2st64_b64 v3, v[24:25], v[28:29] offset0:32 offset1:40
	s_waitcnt vmcnt(16)
	v_cvt_pk_bf16_f32 v32, v32, v33
	v_cvt_pk_bf16_f32 v33, v34, v35
	v_cvt_pk_bf16_f32 v36, v36, v37
	v_cvt_pk_bf16_f32 v37, v38, v39
	ds_write2st64_b64 v3, v[32:33], v[36:37] offset0:48 offset1:56
	s_waitcnt lgkmcnt(0)
	s_or_b32 s41, s22, 0x1000000
	buffer_load_dwordx4 v[8:11], v1, s[4:7], s41 offen sc0 nt
	s_add_u32 s42, s41, 0x4000
	buffer_load_dwordx4 v[12:15], v1, s[4:7], s42 offen sc0 nt
	s_add_u32 s42, s41, 0x8000
	buffer_load_dwordx4 v[16:19], v1, s[4:7], s42 offen sc0 nt
	s_add_u32 s42, s41, 0xc000
	buffer_load_dwordx4 v[20:23], v1, s[4:7], s42 offen sc0 nt
	s_add_u32 s42, s41, 0x10000
	buffer_load_dwordx4 v[24:27], v1, s[4:7], s42 offen sc0 nt
	s_add_u32 s42, s41, 0x14000
	buffer_load_dwordx4 v[28:31], v1, s[4:7], s42 offen sc0 nt
	s_add_u32 s42, s41, 0x18000
	buffer_load_dwordx4 v[32:35], v1, s[4:7], s42 offen sc0 nt
	s_add_u32 s42, s41, 0x1c000
	buffer_load_dwordx4 v[36:39], v1, s[4:7], s42 offen sc0 nt
	s_waitcnt vmcnt(20)
	s_waitcnt lgkmcnt(0)
	s_barrier
	s_cmp_lt_u32 s21, 4
	s_cbranch_scc1 .Lg_nostag
	s_barrier

.Lg_loop:
	v_add_u32_e32 v6, s33, v5
	ds_read_b128 v[72:75], v6 offset:0
	ds_read_b128 v[76:79], v6 offset:2048
	ds_read_b128 v[80:83], v6 offset:4096
	ds_read_b128 v[84:87], v6 offset:6144
	ds_read_b128 v[88:91], v4 offset:0
	ds_read_b128 v[92:95], v4 offset:2048
	ds_read_b128 v[96:99], v4 offset:4096
	ds_read_b128 v[100:103], v4 offset:6144
	ds_read_b128 v[104:107], v4 offset:8192
	ds_read_b128 v[108:111], v4 offset:10240
	ds_read_b128 v[112:115], v4 offset:12288
	ds_read_b128 v[116:119], v4 offset:14336
	s_waitcnt vmcnt(18)
	v_cvt_pk_bf16_f32 v40, v40, v41
	v_cvt_pk_bf16_f32 v41, v42, v43
	v_cvt_pk_bf16_f32 v44, v44, v45
	v_cvt_pk_bf16_f32 v45, v46, v47
	ds_write2st64_b64 v3, v[40:41], v[44:45] offset0:64 offset1:72
	s_waitcnt vmcnt(16)
	v_cvt_pk_bf16_f32 v48, v48, v49
	v_cvt_pk_bf16_f32 v49, v50, v51
	v_cvt_pk_bf16_f32 v52, v52, v53
	v_cvt_pk_bf16_f32 v53, v54, v55
	ds_write2st64_b64 v3, v[48:49], v[52:53] offset0:80 offset1:88
	s_waitcnt vmcnt(14)
	v_cvt_pk_bf16_f32 v56, v56, v57
	v_cvt_pk_bf16_f32 v57, v58, v59
	v_cvt_pk_bf16_f32 v60, v60, v61
	v_cvt_pk_bf16_f32 v61, v62, v63
	ds_write2st64_b64 v3, v[56:57], v[60:61] offset0:96 offset1:104
	s_waitcnt vmcnt(12)
	v_cvt_pk_bf16_f32 v64, v64, v65
	v_cvt_pk_bf16_f32 v65, v66, v67
	v_cvt_pk_bf16_f32 v68, v68, v69
	v_cvt_pk_bf16_f32 v69, v70, v71
	ds_write2st64_b64 v3, v[64:65], v[68:69] offset0:112 offset1:120
	s_waitcnt lgkmcnt(0)
	s_barrier
	s_setprio 1
	s_mov_b32 m0, s26
	s_min_u32 s40, s25, 31
	s_bitcmp1_b32 s40, 4
	s_cselect_b32 s41, s23, s22
	s_lshl_b32 s42, s40, 23
	s_and_b32 s42, s42, 0x7000000
	s_or_b32 s41, s41, s42
	s_lshl_b32 s42, s40, 8
	s_and_b32 s42, s42, 0x100
	s_or_b32 s41, s41, s42
	s_sub_u32 s43, s25, 1
	s_min_u32 s43, s43, 31
	s_and_b32 s43, s43, 15
	s_lshl_b32 s43, s43, 15
	s_add_u32 s44, s43, s24
	v_mfma_f32_16x16x32_bf16 v[120:123], v[72:75], v[88:91], v[120:123]
	v_mfma_f32_16x16x32_bf16 v[124:127], v[76:79], v[88:91], v[124:127]
	buffer_load_dwordx4 v2, s[12:15], s44 offen sc1 lds
	v_mfma_f32_16x16x32_bf16 v[128:131], v[80:83], v[88:91], v[128:131]
	v_mfma_f32_16x16x32_bf16 v[132:135], v[84:87], v[88:91], v[132:135]
	buffer_load_dwordx4 v2, s[12:15], s44 offen offset:1024 sc1 lds
	v_mfma_f32_16x16x32_bf16 v[136:139], v[72:75], v[92:95], v[136:139]
	v_mfma_f32_16x16x32_bf16 v[140:143], v[76:79], v[92:95], v[140:143]
	buffer_load_dwordx4 v2, s[12:15], s44 offen offset:2048 sc1 lds
	v_mfma_f32_16x16x32_bf16 v[144:147], v[80:83], v[92:95], v[144:147]
	v_mfma_f32_16x16x32_bf16 v[148:151], v[84:87], v[92:95], v[148:151]
	buffer_load_dwordx4 v2, s[12:15], s44 offen offset:3072 sc1 lds
	v_mfma_f32_16x16x32_bf16 v[152:155], v[72:75], v[96:99], v[152:155]
	v_mfma_f32_16x16x32_bf16 v[156:159], v[76:79], v[96:99], v[156:159]
	v_mfma_f32_16x16x32_bf16 v[160:163], v[80:83], v[96:99], v[160:163]
	v_mfma_f32_16x16x32_bf16 v[164:167], v[84:87], v[96:99], v[164:167]
	buffer_load_dwordx4 v[40:43], v1, s[4:7], s41 offen sc0 nt
	v_mfma_f32_16x16x32_bf16 v[168:171], v[72:75], v[100:103], v[168:171]
	v_mfma_f32_16x16x32_bf16 v[172:175], v[76:79], v[100:103], v[172:175]
	v_mfma_f32_16x16x32_bf16 v[176:179], v[80:83], v[100:103], v[176:179]
	v_mfma_f32_16x16x32_bf16 v[180:183], v[84:87], v[100:103], v[180:183]
	s_add_u32 s42, s41, 0x4000
	buffer_load_dwordx4 v[44:47], v1, s[4:7], s42 offen sc0 nt
	v_mfma_f32_16x16x32_bf16 v[184:187], v[72:75], v[104:107], v[184:187]
	v_mfma_f32_16x16x32_bf16 v[188:191], v[76:79], v[104:107], v[188:191]
	v_mfma_f32_16x16x32_bf16 v[192:195], v[80:83], v[104:107], v[192:195]
	v_mfma_f32_16x16x32_bf16 v[196:199], v[84:87], v[104:107], v[196:199]
	s_add_u32 s42, s41, 0x8000
	buffer_load_dwordx4 v[48:51], v1, s[4:7], s42 offen sc0 nt
	v_mfma_f32_16x16x32_bf16 v[200:203], v[72:75], v[108:111], v[200:203]
	v_mfma_f32_16x16x32_bf16 v[204:207], v[76:79], v[108:111], v[204:207]
	v_mfma_f32_16x16x32_bf16 v[208:211], v[80:83], v[108:111], v[208:211]
	v_mfma_f32_16x16x32_bf16 v[212:215], v[84:87], v[108:111], v[212:215]
	s_add_u32 s42, s41, 0xc000
	buffer_load_dwordx4 v[52:55], v1, s[4:7], s42 offen sc0 nt
	v_mfma_f32_16x16x32_bf16 v[216:219], v[72:75], v[112:115], v[216:219]
	v_mfma_f32_16x16x32_bf16 v[220:223], v[76:79], v[112:115], v[220:223]
	v_mfma_f32_16x16x32_bf16 v[224:227], v[80:83], v[112:115], v[224:227]
	v_mfma_f32_16x16x32_bf16 v[228:231], v[84:87], v[112:115], v[228:231]
	v_mfma_f32_16x16x32_bf16 v[232:235], v[72:75], v[116:119], v[232:235]
	v_mfma_f32_16x16x32_bf16 v[236:239], v[76:79], v[116:119], v[236:239]
	v_mfma_f32_16x16x32_bf16 v[240:243], v[80:83], v[116:119], v[240:243]
	v_mfma_f32_16x16x32_bf16 v[244:247], v[84:87], v[116:119], v[244:247]
	s_add_u32 s26, s26, 0x8000
	s_cmp_eq_u32 s26, s32
	s_cselect_b32 s26, s27, s26
	s_setprio 0
	s_barrier
	ds_read_b128 v[72:75], v6 offset:1024
	ds_read_b128 v[76:79], v6 offset:3072
	ds_read_b128 v[80:83], v6 offset:5120
	ds_read_b128 v[84:87], v6 offset:7168
	ds_read_b128 v[88:91], v252 offset:1024
	ds_read_b128 v[92:95], v252 offset:3072
	ds_read_b128 v[96:99], v252 offset:5120
	ds_read_b128 v[100:103], v252 offset:7168
	ds_read_b128 v[104:107], v252 offset:9216
	ds_read_b128 v[108:111], v252 offset:11264
	ds_read_b128 v[112:115], v252 offset:13312
	ds_read_b128 v[116:119], v252 offset:15360
	s_waitcnt vmcnt(16)
	s_waitcnt lgkmcnt(0)
	s_barrier
	s_setprio 1
	s_add_u32 s33, s33, 0x8000
	s_cmp_eq_u32 s33, 0x18000
	s_cselect_b32 s33, 0, s33
	s_add_u32 s25, s25, 1
	v_mfma_f32_16x16x32_bf16 v[120:123], v[72:75], v[88:91], v[120:123]
	v_mfma_f32_16x16x32_bf16 v[124:127], v[76:79], v[88:91], v[124:127]
	v_mfma_f32_16x16x32_bf16 v[128:131], v[80:83], v[88:91], v[128:131]
	v_mfma_f32_16x16x32_bf16 v[132:135], v[84:87], v[88:91], v[132:135]
	s_add_u32 s42, s41, 0x10000
	buffer_load_dwordx4 v[56:59], v1, s[4:7], s42 offen sc0 nt
	v_mfma_f32_16x16x32_bf16 v[136:139], v[72:75], v[92:95], v[136:139]
	v_mfma_f32_16x16x32_bf16 v[140:143], v[76:79], v[92:95], v[140:143]
	v_mfma_f32_16x16x32_bf16 v[144:147], v[80:83], v[92:95], v[144:147]
	v_mfma_f32_16x16x32_bf16 v[148:151], v[84:87], v[92:95], v[148:151]
	v_mfma_f32_16x16x32_bf16 v[152:155], v[72:75], v[96:99], v[152:155]
	v_mfma_f32_16x16x32_bf16 v[156:159], v[76:79], v[96:99], v[156:159]
	v_mfma_f32_16x16x32_bf16 v[160:163], v[80:83], v[96:99], v[160:163]
	v_mfma_f32_16x16x32_bf16 v[164:167], v[84:87], v[96:99], v[164:167]
	s_add_u32 s42, s41, 0x14000
	buffer_load_dwordx4 v[60:63], v1, s[4:7], s42 offen sc0 nt
	v_mfma_f32_16x16x32_bf16 v[168:171], v[72:75], v[100:103], v[168:171]
	v_mfma_f32_16x16x32_bf16 v[172:175], v[76:79], v[100:103], v[172:175]
	v_mfma_f32_16x16x32_bf16 v[176:179], v[80:83], v[100:103], v[176:179]
	v_mfma_f32_16x16x32_bf16 v[180:183], v[84:87], v[100:103], v[180:183]
	v_mfma_f32_16x16x32_bf16 v[184:187], v[72:75], v[104:107], v[184:187]
	v_mfma_f32_16x16x32_bf16 v[188:191], v[76:79], v[104:107], v[188:191]
	v_mfma_f32_16x16x32_bf16 v[192:195], v[80:83], v[104:107], v[192:195]
	v_mfma_f32_16x16x32_bf16 v[196:199], v[84:87], v[104:107], v[196:199]
	s_add_u32 s42, s41, 0x18000
	buffer_load_dwordx4 v[64:67], v1, s[4:7], s42 offen sc0 nt
	v_mfma_f32_16x16x32_bf16 v[200:203], v[72:75], v[108:111], v[200:203]
	v_mfma_f32_16x16x32_bf16 v[204:207], v[76:79], v[108:111], v[204:207]
	v_mfma_f32_16x16x32_bf16 v[208:211], v[80:83], v[108:111], v[208:211]
	v_mfma_f32_16x16x32_bf16 v[212:215], v[84:87], v[108:111], v[212:215]
	v_mfma_f32_16x16x32_bf16 v[216:219], v[72:75], v[112:115], v[216:219]
	v_mfma_f32_16x16x32_bf16 v[220:223], v[76:79], v[112:115], v[220:223]
	v_mfma_f32_16x16x32_bf16 v[224:227], v[80:83], v[112:115], v[224:227]
	v_mfma_f32_16x16x32_bf16 v[228:231], v[84:87], v[112:115], v[228:231]
	s_add_u32 s42, s41, 0x1c000
	buffer_load_dwordx4 v[68:71], v1, s[4:7], s42 offen sc0 nt
	v_mfma_f32_16x16x32_bf16 v[232:235], v[72:75], v[116:119], v[232:235]
	v_mfma_f32_16x16x32_bf16 v[236:239], v[76:79], v[116:119], v[236:239]
	v_mfma_f32_16x16x32_bf16 v[240:243], v[80:83], v[116:119], v[240:243]
	v_mfma_f32_16x16x32_bf16 v[244:247], v[84:87], v[116:119], v[244:247]
	s_setprio 0
	s_barrier
	v_add_u32_e32 v6, s33, v5
	ds_read_b128 v[72:75], v6 offset:0
	ds_read_b128 v[76:79], v6 offset:2048
	ds_read_b128 v[80:83], v6 offset:4096
	ds_read_b128 v[84:87], v6 offset:6144
	ds_read_b128 v[88:91], v4 offset:32768
	ds_read_b128 v[92:95], v4 offset:34816
	ds_read_b128 v[96:99], v4 offset:36864
	ds_read_b128 v[100:103], v4 offset:38912
	ds_read_b128 v[104:107], v4 offset:40960
	ds_read_b128 v[108:111], v4 offset:43008
	ds_read_b128 v[112:115], v4 offset:45056
	ds_read_b128 v[116:119], v4 offset:47104
	s_waitcnt vmcnt(18)
	v_cvt_pk_bf16_f32 v8, v8, v9
	v_cvt_pk_bf16_f32 v9, v10, v11
	v_cvt_pk_bf16_f32 v12, v12, v13
	v_cvt_pk_bf16_f32 v13, v14, v15
	ds_write2st64_b64 v3, v[8:9], v[12:13] offset0:0 offset1:8
	s_waitcnt vmcnt(16)
	v_cvt_pk_bf16_f32 v16, v16, v17
	v_cvt_pk_bf16_f32 v17, v18, v19
	v_cvt_pk_bf16_f32 v20, v20, v21
	v_cvt_pk_bf16_f32 v21, v22, v23
	ds_write2st64_b64 v3, v[16:17], v[20:21] offset0:16 offset1:24
	s_waitcnt vmcnt(14)
	v_cvt_pk_bf16_f32 v24, v24, v25
	v_cvt_pk_bf16_f32 v25, v26, v27
	v_cvt_pk_bf16_f32 v28, v28, v29
	v_cvt_pk_bf16_f32 v29, v30, v31
	ds_write2st64_b64 v3, v[24:25], v[28:29] offset0:32 offset1:40
	s_waitcnt vmcnt(12)
	v_cvt_pk_bf16_f32 v32, v32, v33
	v_cvt_pk_bf16_f32 v33, v34, v35
	v_cvt_pk_bf16_f32 v36, v36, v37
	v_cvt_pk_bf16_f32 v37, v38, v39
	ds_write2st64_b64 v3, v[32:33], v[36:37] offset0:48 offset1:56
	s_waitcnt lgkmcnt(0)
	s_barrier
	s_setprio 1
	s_mov_b32 m0, s26
	s_min_u32 s40, s25, 31
	s_bitcmp1_b32 s40, 4
	s_cselect_b32 s41, s23, s22
	s_lshl_b32 s42, s40, 23
	s_and_b32 s42, s42, 0x7000000
	s_or_b32 s41, s41, s42
	s_lshl_b32 s42, s40, 8
	s_and_b32 s42, s42, 0x100
	s_or_b32 s41, s41, s42
	s_sub_u32 s43, s25, 1
	s_min_u32 s43, s43, 31
	s_and_b32 s43, s43, 15
	s_lshl_b32 s43, s43, 15
	s_add_u32 s44, s43, s24
	v_mfma_f32_16x16x32_bf16 v[120:123], v[72:75], v[88:91], v[120:123]
	v_mfma_f32_16x16x32_bf16 v[124:127], v[76:79], v[88:91], v[124:127]
	buffer_load_dwordx4 v2, s[12:15], s44 offen sc1 lds
	v_mfma_f32_16x16x32_bf16 v[128:131], v[80:83], v[88:91], v[128:131]
	v_mfma_f32_16x16x32_bf16 v[132:135], v[84:87], v[88:91], v[132:135]
	buffer_load_dwordx4 v2, s[12:15], s44 offen offset:1024 sc1 lds
	v_mfma_f32_16x16x32_bf16 v[136:139], v[72:75], v[92:95], v[136:139]
	v_mfma_f32_16x16x32_bf16 v[140:143], v[76:79], v[92:95], v[140:143]
	buffer_load_dwordx4 v2, s[12:15], s44 offen offset:2048 sc1 lds
	v_mfma_f32_16x16x32_bf16 v[144:147], v[80:83], v[92:95], v[144:147]
	v_mfma_f32_16x16x32_bf16 v[148:151], v[84:87], v[92:95], v[148:151]
	buffer_load_dwordx4 v2, s[12:15], s44 offen offset:3072 sc1 lds
	v_mfma_f32_16x16x32_bf16 v[152:155], v[72:75], v[96:99], v[152:155]
	v_mfma_f32_16x16x32_bf16 v[156:159], v[76:79], v[96:99], v[156:159]
	v_mfma_f32_16x16x32_bf16 v[160:163], v[80:83], v[96:99], v[160:163]
	v_mfma_f32_16x16x32_bf16 v[164:167], v[84:87], v[96:99], v[164:167]
	buffer_load_dwordx4 v[8:11], v1, s[4:7], s41 offen sc0 nt
	v_mfma_f32_16x16x32_bf16 v[168:171], v[72:75], v[100:103], v[168:171]
	v_mfma_f32_16x16x32_bf16 v[172:175], v[76:79], v[100:103], v[172:175]
	v_mfma_f32_16x16x32_bf16 v[176:179], v[80:83], v[100:103], v[176:179]
	v_mfma_f32_16x16x32_bf16 v[180:183], v[84:87], v[100:103], v[180:183]
	s_add_u32 s42, s41, 0x4000
	buffer_load_dwordx4 v[12:15], v1, s[4:7], s42 offen sc0 nt
	v_mfma_f32_16x16x32_bf16 v[184:187], v[72:75], v[104:107], v[184:187]
	v_mfma_f32_16x16x32_bf16 v[188:191], v[76:79], v[104:107], v[188:191]
	v_mfma_f32_16x16x32_bf16 v[192:195], v[80:83], v[104:107], v[192:195]
	v_mfma_f32_16x16x32_bf16 v[196:199], v[84:87], v[104:107], v[196:199]
	s_add_u32 s42, s41, 0x8000
	buffer_load_dwordx4 v[16:19], v1, s[4:7], s42 offen sc0 nt
	v_mfma_f32_16x16x32_bf16 v[200:203], v[72:75], v[108:111], v[200:203]
	v_mfma_f32_16x16x32_bf16 v[204:207], v[76:79], v[108:111], v[204:207]
	v_mfma_f32_16x16x32_bf16 v[208:211], v[80:83], v[108:111], v[208:211]
	v_mfma_f32_16x16x32_bf16 v[212:215], v[84:87], v[108:111], v[212:215]
	s_add_u32 s42, s41, 0xc000
	buffer_load_dwordx4 v[20:23], v1, s[4:7], s42 offen sc0 nt
	v_mfma_f32_16x16x32_bf16 v[216:219], v[72:75], v[112:115], v[216:219]
	v_mfma_f32_16x16x32_bf16 v[220:223], v[76:79], v[112:115], v[220:223]
	v_mfma_f32_16x16x32_bf16 v[224:227], v[80:83], v[112:115], v[224:227]
	v_mfma_f32_16x16x32_bf16 v[228:231], v[84:87], v[112:115], v[228:231]
	v_mfma_f32_16x16x32_bf16 v[232:235], v[72:75], v[116:119], v[232:235]
	v_mfma_f32_16x16x32_bf16 v[236:239], v[76:79], v[116:119], v[236:239]
	v_mfma_f32_16x16x32_bf16 v[240:243], v[80:83], v[116:119], v[240:243]
	v_mfma_f32_16x16x32_bf16 v[244:247], v[84:87], v[116:119], v[244:247]
	s_add_u32 s26, s26, 0x8000
	s_cmp_eq_u32 s26, s32
	s_cselect_b32 s26, s27, s26
	s_setprio 0
	s_barrier
	ds_read_b128 v[72:75], v6 offset:1024
	ds_read_b128 v[76:79], v6 offset:3072
	ds_read_b128 v[80:83], v6 offset:5120
	ds_read_b128 v[84:87], v6 offset:7168
	ds_read_b128 v[88:91], v252 offset:33792
	ds_read_b128 v[92:95], v252 offset:35840
	ds_read_b128 v[96:99], v252 offset:37888
	ds_read_b128 v[100:103], v252 offset:39936
	ds_read_b128 v[104:107], v252 offset:41984
	ds_read_b128 v[108:111], v252 offset:44032
	ds_read_b128 v[112:115], v252 offset:46080
	ds_read_b128 v[116:119], v252 offset:48128
	s_waitcnt vmcnt(16)
	s_waitcnt lgkmcnt(0)
	s_barrier
	s_setprio 1
	s_add_u32 s33, s33, 0x8000
	s_cmp_eq_u32 s33, 0x18000
	s_cselect_b32 s33, 0, s33
	s_add_u32 s25, s25, 1
	v_mfma_f32_16x16x32_bf16 v[120:123], v[72:75], v[88:91], v[120:123]
	v_mfma_f32_16x16x32_bf16 v[124:127], v[76:79], v[88:91], v[124:127]
	v_mfma_f32_16x16x32_bf16 v[128:131], v[80:83], v[88:91], v[128:131]
	v_mfma_f32_16x16x32_bf16 v[132:135], v[84:87], v[88:91], v[132:135]
	s_add_u32 s42, s41, 0x10000
	buffer_load_dwordx4 v[24:27], v1, s[4:7], s42 offen sc0 nt
	v_mfma_f32_16x16x32_bf16 v[136:139], v[72:75], v[92:95], v[136:139]
	v_mfma_f32_16x16x32_bf16 v[140:143], v[76:79], v[92:95], v[140:143]
	v_mfma_f32_16x16x32_bf16 v[144:147], v[80:83], v[92:95], v[144:147]
	v_mfma_f32_16x16x32_bf16 v[148:151], v[84:87], v[92:95], v[148:151]
	v_mfma_f32_16x16x32_bf16 v[152:155], v[72:75], v[96:99], v[152:155]
	v_mfma_f32_16x16x32_bf16 v[156:159], v[76:79], v[96:99], v[156:159]
	v_mfma_f32_16x16x32_bf16 v[160:163], v[80:83], v[96:99], v[160:163]
	v_mfma_f32_16x16x32_bf16 v[164:167], v[84:87], v[96:99], v[164:167]
	s_add_u32 s42, s41, 0x14000
	buffer_load_dwordx4 v[28:31], v1, s[4:7], s42 offen sc0 nt
	v_mfma_f32_16x16x32_bf16 v[168:171], v[72:75], v[100:103], v[168:171]
	v_mfma_f32_16x16x32_bf16 v[172:175], v[76:79], v[100:103], v[172:175]
	v_mfma_f32_16x16x32_bf16 v[176:179], v[80:83], v[100:103], v[176:179]
	v_mfma_f32_16x16x32_bf16 v[180:183], v[84:87], v[100:103], v[180:183]
	v_mfma_f32_16x16x32_bf16 v[184:187], v[72:75], v[104:107], v[184:187]
	v_mfma_f32_16x16x32_bf16 v[188:191], v[76:79], v[104:107], v[188:191]
	v_mfma_f32_16x16x32_bf16 v[192:195], v[80:83], v[104:107], v[192:195]
	v_mfma_f32_16x16x32_bf16 v[196:199], v[84:87], v[104:107], v[196:199]
	s_add_u32 s42, s41, 0x18000
	buffer_load_dwordx4 v[32:35], v1, s[4:7], s42 offen sc0 nt
	v_mfma_f32_16x16x32_bf16 v[200:203], v[72:75], v[108:111], v[200:203]
	v_mfma_f32_16x16x32_bf16 v[204:207], v[76:79], v[108:111], v[204:207]
	v_mfma_f32_16x16x32_bf16 v[208:211], v[80:83], v[108:111], v[208:211]
	v_mfma_f32_16x16x32_bf16 v[212:215], v[84:87], v[108:111], v[212:215]
	v_mfma_f32_16x16x32_bf16 v[216:219], v[72:75], v[112:115], v[216:219]
	v_mfma_f32_16x16x32_bf16 v[220:223], v[76:79], v[112:115], v[220:223]
	v_mfma_f32_16x16x32_bf16 v[224:227], v[80:83], v[112:115], v[224:227]
	v_mfma_f32_16x16x32_bf16 v[228:231], v[84:87], v[112:115], v[228:231]
	s_add_u32 s42, s41, 0x1c000
	buffer_load_dwordx4 v[36:39], v1, s[4:7], s42 offen sc0 nt
	v_mfma_f32_16x16x32_bf16 v[232:235], v[72:75], v[116:119], v[232:235]
	v_mfma_f32_16x16x32_bf16 v[236:239], v[76:79], v[116:119], v[236:239]
	v_mfma_f32_16x16x32_bf16 v[240:243], v[80:83], v[116:119], v[240:243]
	v_mfma_f32_16x16x32_bf16 v[244:247], v[84:87], v[116:119], v[244:247]
	s_setprio 0
	s_barrier
	s_sub_u32 s38, s38, 1
	s_cmp_lg_u32 s38, 0
	s_cbranch_scc1 .Lg_loop
	s_cmp_lg_u32 s39, 0
	s_cbranch_scc1 .Lg_final
	v_add_u32_e32 v6, s33, v5
	ds_read_b128 v[72:75], v6 offset:0
	ds_read_b128 v[76:79], v6 offset:2048
	ds_read_b128 v[80:83], v6 offset:4096
	ds_read_b128 v[84:87], v6 offset:6144
	ds_read_b128 v[88:91], v4 offset:0
	ds_read_b128 v[92:95], v4 offset:2048
	ds_read_b128 v[96:99], v4 offset:4096
	ds_read_b128 v[100:103], v4 offset:6144
	ds_read_b128 v[104:107], v4 offset:8192
	ds_read_b128 v[108:111], v4 offset:10240
	ds_read_b128 v[112:115], v4 offset:12288
	ds_read_b128 v[116:119], v4 offset:14336
	s_waitcnt vmcnt(18)
	v_cvt_pk_bf16_f32 v40, v40, v41
	v_cvt_pk_bf16_f32 v41, v42, v43
	v_cvt_pk_bf16_f32 v44, v44, v45
	v_cvt_pk_bf16_f32 v45, v46, v47
	ds_write2st64_b64 v3, v[40:41], v[44:45] offset0:64 offset1:72
	s_waitcnt vmcnt(16)
	v_cvt_pk_bf16_f32 v48, v48, v49
	v_cvt_pk_bf16_f32 v49, v50, v51
	v_cvt_pk_bf16_f32 v52, v52, v53
	v_cvt_pk_bf16_f32 v53, v54, v55
	ds_write2st64_b64 v3, v[48:49], v[52:53] offset0:80 offset1:88
	s_waitcnt vmcnt(14)
	v_cvt_pk_bf16_f32 v56, v56, v57
	v_cvt_pk_bf16_f32 v57, v58, v59
	v_cvt_pk_bf16_f32 v60, v60, v61
	v_cvt_pk_bf16_f32 v61, v62, v63
	ds_write2st64_b64 v3, v[56:57], v[60:61] offset0:96 offset1:104
	s_waitcnt vmcnt(12)
	v_cvt_pk_bf16_f32 v64, v64, v65
	v_cvt_pk_bf16_f32 v65, v66, v67
	v_cvt_pk_bf16_f32 v68, v68, v69
	v_cvt_pk_bf16_f32 v69, v70, v71
	ds_write2st64_b64 v3, v[64:65], v[68:69] offset0:112 offset1:120
	s_waitcnt lgkmcnt(0)
	global_load_dwordx4 v[40:43], v249, s[34:35] offset:0
	global_load_dwordx4 v[44:47], v249, s[34:35] offset:64
	global_load_dwordx4 v[48:51], v249, s[34:35] offset:128
	global_load_dwordx4 v[52:55], v249, s[34:35] offset:192
	s_barrier
	s_setprio 1
	s_mov_b32 m0, s26
	s_min_u32 s40, s25, 31
	s_bitcmp1_b32 s40, 4
	s_cselect_b32 s41, s23, s22
	s_lshl_b32 s42, s40, 23
	s_and_b32 s42, s42, 0x7000000
	s_or_b32 s41, s41, s42
	s_lshl_b32 s42, s40, 8
	s_and_b32 s42, s42, 0x100
	s_or_b32 s41, s41, s42
	s_sub_u32 s43, s25, 1
	s_min_u32 s43, s43, 31
	s_and_b32 s43, s43, 15
	s_lshl_b32 s43, s43, 15
	s_add_u32 s44, s43, s24
	buffer_load_dwordx4 v2, s[12:15], s44 offen sc1 lds
	buffer_load_dwordx4 v2, s[12:15], s44 offen offset:1024 sc1 lds
	buffer_load_dwordx4 v2, s[12:15], s44 offen offset:2048 sc1 lds
	buffer_load_dwordx4 v2, s[12:15], s44 offen offset:3072 sc1 lds
	s_waitcnt vmcnt(4)
	s_mov_b32 s45, s36
	buffer_store_dwordx4 v[120:123], v248, s[28:31], s45 offen
	buffer_store_dwordx4 v[124:127], v248, s[28:31], s45 offen offset:64
	v_mfma_f32_16x16x32_bf16 v[120:123], v[72:75], v[88:91], v[40:43]
	buffer_store_dwordx4 v[128:131], v248, s[28:31], s45 offen offset:128
	v_mfma_f32_16x16x32_bf16 v[124:127], v[76:79], v[88:91], v[44:47]
	buffer_store_dwordx4 v[132:135], v248, s[28:31], s45 offen offset:192
	v_mfma_f32_16x16x32_bf16 v[128:131], v[80:83], v[88:91], v[48:51]
	s_add_u32 s45, s36, 0x2000
	buffer_store_dwordx4 v[136:139], v248, s[28:31], s45 offen
	v_mfma_f32_16x16x32_bf16 v[132:135], v[84:87], v[88:91], v[52:55]
	buffer_store_dwordx4 v[140:143], v248, s[28:31], s45 offen offset:64
	v_mfma_f32_16x16x32_bf16 v[136:139], v[72:75], v[92:95], v[40:43]
	buffer_store_dwordx4 v[144:147], v248, s[28:31], s45 offen offset:128
	v_mfma_f32_16x16x32_bf16 v[140:143], v[76:79], v[92:95], v[44:47]
	buffer_store_dwordx4 v[148:151], v248, s[28:31], s45 offen offset:192
	v_mfma_f32_16x16x32_bf16 v[144:147], v[80:83], v[92:95], v[48:51]
	s_add_u32 s45, s36, 0x4000
	buffer_store_dwordx4 v[152:155], v248, s[28:31], s45 offen
	v_mfma_f32_16x16x32_bf16 v[148:151], v[84:87], v[92:95], v[52:55]
	buffer_store_dwordx4 v[156:159], v248, s[28:31], s45 offen offset:64
	v_mfma_f32_16x16x32_bf16 v[152:155], v[72:75], v[96:99], v[40:43]
	buffer_store_dwordx4 v[160:163], v248, s[28:31], s45 offen offset:128
	v_mfma_f32_16x16x32_bf16 v[156:159], v[76:79], v[96:99], v[44:47]
	buffer_store_dwordx4 v[164:167], v248, s[28:31], s45 offen offset:192
	v_mfma_f32_16x16x32_bf16 v[160:163], v[80:83], v[96:99], v[48:51]
	s_add_u32 s45, s36, 0x6000
	buffer_store_dwordx4 v[168:171], v248, s[28:31], s45 offen
	v_mfma_f32_16x16x32_bf16 v[164:167], v[84:87], v[96:99], v[52:55]
	buffer_store_dwordx4 v[172:175], v248, s[28:31], s45 offen offset:64
	v_mfma_f32_16x16x32_bf16 v[168:171], v[72:75], v[100:103], v[40:43]
	buffer_store_dwordx4 v[176:179], v248, s[28:31], s45 offen offset:128
	v_mfma_f32_16x16x32_bf16 v[172:175], v[76:79], v[100:103], v[44:47]
	buffer_store_dwordx4 v[180:183], v248, s[28:31], s45 offen offset:192
	v_mfma_f32_16x16x32_bf16 v[176:179], v[80:83], v[100:103], v[48:51]
	s_add_u32 s45, s36, 0x8000
	buffer_store_dwordx4 v[184:187], v248, s[28:31], s45 offen
	v_mfma_f32_16x16x32_bf16 v[180:183], v[84:87], v[100:103], v[52:55]
	buffer_store_dwordx4 v[188:191], v248, s[28:31], s45 offen offset:64
	v_mfma_f32_16x16x32_bf16 v[184:187], v[72:75], v[104:107], v[40:43]
	buffer_store_dwordx4 v[192:195], v248, s[28:31], s45 offen offset:128
	v_mfma_f32_16x16x32_bf16 v[188:191], v[76:79], v[104:107], v[44:47]
	buffer_store_dwordx4 v[196:199], v248, s[28:31], s45 offen offset:192
	v_mfma_f32_16x16x32_bf16 v[192:195], v[80:83], v[104:107], v[48:51]
	s_add_u32 s45, s36, 0xa000
	buffer_store_dwordx4 v[200:203], v248, s[28:31], s45 offen
	v_mfma_f32_16x16x32_bf16 v[196:199], v[84:87], v[104:107], v[52:55]
	buffer_store_dwordx4 v[204:207], v248, s[28:31], s45 offen offset:64
	v_mfma_f32_16x16x32_bf16 v[200:203], v[72:75], v[108:111], v[40:43]
	buffer_store_dwordx4 v[208:211], v248, s[28:31], s45 offen offset:128
	v_mfma_f32_16x16x32_bf16 v[204:207], v[76:79], v[108:111], v[44:47]
	buffer_store_dwordx4 v[212:215], v248, s[28:31], s45 offen offset:192
	v_mfma_f32_16x16x32_bf16 v[208:211], v[80:83], v[108:111], v[48:51]
	s_add_u32 s45, s36, 0xc000
	buffer_store_dwordx4 v[216:219], v248, s[28:31], s45 offen
	v_mfma_f32_16x16x32_bf16 v[212:215], v[84:87], v[108:111], v[52:55]
	buffer_store_dwordx4 v[220:223], v248, s[28:31], s45 offen offset:64
	v_mfma_f32_16x16x32_bf16 v[216:219], v[72:75], v[112:115], v[40:43]
	buffer_store_dwordx4 v[224:227], v248, s[28:31], s45 offen offset:128
	v_mfma_f32_16x16x32_bf16 v[220:223], v[76:79], v[112:115], v[44:47]
	buffer_store_dwordx4 v[228:231], v248, s[28:31], s45 offen offset:192
	v_mfma_f32_16x16x32_bf16 v[224:227], v[80:83], v[112:115], v[48:51]
	s_add_u32 s45, s36, 0xe000
	buffer_store_dwordx4 v[232:235], v248, s[28:31], s45 offen
	v_mfma_f32_16x16x32_bf16 v[228:231], v[84:87], v[112:115], v[52:55]
	buffer_store_dwordx4 v[236:239], v248, s[28:31], s45 offen offset:64
	v_mfma_f32_16x16x32_bf16 v[232:235], v[72:75], v[116:119], v[40:43]
	buffer_store_dwordx4 v[240:243], v248, s[28:31], s45 offen offset:128
	v_mfma_f32_16x16x32_bf16 v[236:239], v[76:79], v[116:119], v[44:47]
	buffer_store_dwordx4 v[244:247], v248, s[28:31], s45 offen offset:192
	v_mfma_f32_16x16x32_bf16 v[240:243], v[80:83], v[116:119], v[48:51]
	v_mfma_f32_16x16x32_bf16 v[244:247], v[84:87], v[116:119], v[52:55]
	s_add_u32 s26, s26, 0x8000
	s_cmp_eq_u32 s26, s32
	s_cselect_b32 s26, s27, s26
	s_setprio 0
	s_barrier
	ds_read_b128 v[72:75], v6 offset:1024
	ds_read_b128 v[76:79], v6 offset:3072
	ds_read_b128 v[80:83], v6 offset:5120
	ds_read_b128 v[84:87], v6 offset:7168
	ds_read_b128 v[88:91], v252 offset:1024
	ds_read_b128 v[92:95], v252 offset:3072
	ds_read_b128 v[96:99], v252 offset:5120
	ds_read_b128 v[100:103], v252 offset:7168
	ds_read_b128 v[104:107], v252 offset:9216
	ds_read_b128 v[108:111], v252 offset:11264
	ds_read_b128 v[112:115], v252 offset:13312
	ds_read_b128 v[116:119], v252 offset:15360
	s_waitcnt vmcnt(48)
	s_waitcnt lgkmcnt(0)
	s_barrier
	s_setprio 1
	s_add_u32 s33, s33, 0x8000
	s_cmp_eq_u32 s33, 0x18000
	s_cselect_b32 s33, 0, s33
	s_add_u32 s25, s25, 1
	v_mfma_f32_16x16x32_bf16 v[120:123], v[72:75], v[88:91], v[120:123]
	v_mfma_f32_16x16x32_bf16 v[124:127], v[76:79], v[88:91], v[124:127]
	v_mfma_f32_16x16x32_bf16 v[128:131], v[80:83], v[88:91], v[128:131]
	buffer_load_dwordx4 v[40:43], v1, s[4:7], s41 offen sc0 nt
	v_mfma_f32_16x16x32_bf16 v[132:135], v[84:87], v[88:91], v[132:135]
	v_mfma_f32_16x16x32_bf16 v[136:139], v[72:75], v[92:95], v[136:139]
	v_mfma_f32_16x16x32_bf16 v[140:143], v[76:79], v[92:95], v[140:143]
	v_mfma_f32_16x16x32_bf16 v[144:147], v[80:83], v[92:95], v[144:147]
	s_add_u32 s42, s41, 0x4000
	buffer_load_dwordx4 v[44:47], v1, s[4:7], s42 offen sc0 nt
	v_mfma_f32_16x16x32_bf16 v[148:151], v[84:87], v[92:95], v[148:151]
	v_mfma_f32_16x16x32_bf16 v[152:155], v[72:75], v[96:99], v[152:155]
	v_mfma_f32_16x16x32_bf16 v[156:159], v[76:79], v[96:99], v[156:159]
	v_mfma_f32_16x16x32_bf16 v[160:163], v[80:83], v[96:99], v[160:163]
	s_add_u32 s42, s41, 0x8000
	buffer_load_dwordx4 v[48:51], v1, s[4:7], s42 offen sc0 nt
	v_mfma_f32_16x16x32_bf16 v[164:167], v[84:87], v[96:99], v[164:167]
	v_mfma_f32_16x16x32_bf16 v[168:171], v[72:75], v[100:103], v[168:171]
	v_mfma_f32_16x16x32_bf16 v[172:175], v[76:79], v[100:103], v[172:175]
	v_mfma_f32_16x16x32_bf16 v[176:179], v[80:83], v[100:103], v[176:179]
	s_add_u32 s42, s41, 0xc000
	buffer_load_dwordx4 v[52:55], v1, s[4:7], s42 offen sc0 nt
	v_mfma_f32_16x16x32_bf16 v[180:183], v[84:87], v[100:103], v[180:183]
	v_mfma_f32_16x16x32_bf16 v[184:187], v[72:75], v[104:107], v[184:187]
	v_mfma_f32_16x16x32_bf16 v[188:191], v[76:79], v[104:107], v[188:191]
	v_mfma_f32_16x16x32_bf16 v[192:195], v[80:83], v[104:107], v[192:195]
	s_add_u32 s42, s41, 0x10000
	buffer_load_dwordx4 v[56:59], v1, s[4:7], s42 offen sc0 nt
	v_mfma_f32_16x16x32_bf16 v[196:199], v[84:87], v[104:107], v[196:199]
	v_mfma_f32_16x16x32_bf16 v[200:203], v[72:75], v[108:111], v[200:203]
	v_mfma_f32_16x16x32_bf16 v[204:207], v[76:79], v[108:111], v[204:207]
	v_mfma_f32_16x16x32_bf16 v[208:211], v[80:83], v[108:111], v[208:211]
	s_add_u32 s42, s41, 0x14000
	buffer_load_dwordx4 v[60:63], v1, s[4:7], s42 offen sc0 nt
	v_mfma_f32_16x16x32_bf16 v[212:215], v[84:87], v[108:111], v[212:215]
	v_mfma_f32_16x16x32_bf16 v[216:219], v[72:75], v[112:115], v[216:219]
	v_mfma_f32_16x16x32_bf16 v[220:223], v[76:79], v[112:115], v[220:223]
	v_mfma_f32_16x16x32_bf16 v[224:227], v[80:83], v[112:115], v[224:227]
	s_add_u32 s42, s41, 0x18000
	buffer_load_dwordx4 v[64:67], v1, s[4:7], s42 offen sc0 nt
	v_mfma_f32_16x16x32_bf16 v[228:231], v[84:87], v[112:115], v[228:231]
	v_mfma_f32_16x16x32_bf16 v[232:235], v[72:75], v[116:119], v[232:235]
	v_mfma_f32_16x16x32_bf16 v[236:239], v[76:79], v[116:119], v[236:239]
	v_mfma_f32_16x16x32_bf16 v[240:243], v[80:83], v[116:119], v[240:243]
	s_add_u32 s42, s41, 0x1c000
	buffer_load_dwordx4 v[68:71], v1, s[4:7], s42 offen sc0 nt
	v_mfma_f32_16x16x32_bf16 v[244:247], v[84:87], v[116:119], v[244:247]
	s_setprio 0
	s_barrier
	v_add_u32_e32 v6, s33, v5
	ds_read_b128 v[72:75], v6 offset:0
	ds_read_b128 v[76:79], v6 offset:2048
	ds_read_b128 v[80:83], v6 offset:4096
	ds_read_b128 v[84:87], v6 offset:6144
	ds_read_b128 v[88:91], v4 offset:32768
	ds_read_b128 v[92:95], v4 offset:34816
	ds_read_b128 v[96:99], v4 offset:36864
	ds_read_b128 v[100:103], v4 offset:38912
	ds_read_b128 v[104:107], v4 offset:40960
	ds_read_b128 v[108:111], v4 offset:43008
	ds_read_b128 v[112:115], v4 offset:45056
	ds_read_b128 v[116:119], v4 offset:47104
	s_waitcnt vmcnt(54)
	v_cvt_pk_bf16_f32 v8, v8, v9
	v_cvt_pk_bf16_f32 v9, v10, v11
	v_cvt_pk_bf16_f32 v12, v12, v13
	v_cvt_pk_bf16_f32 v13, v14, v15
	ds_write2st64_b64 v3, v[8:9], v[12:13] offset0:0 offset1:8
	s_waitcnt vmcnt(52)
	v_cvt_pk_bf16_f32 v16, v16, v17
	v_cvt_pk_bf16_f32 v17, v18, v19
	v_cvt_pk_bf16_f32 v20, v20, v21
	v_cvt_pk_bf16_f32 v21, v22, v23
	ds_write2st64_b64 v3, v[16:17], v[20:21] offset0:16 offset1:24
	s_waitcnt vmcnt(50)
	v_cvt_pk_bf16_f32 v24, v24, v25
	v_cvt_pk_bf16_f32 v25, v26, v27
	v_cvt_pk_bf16_f32 v28, v28, v29
	v_cvt_pk_bf16_f32 v29, v30, v31
	ds_write2st64_b64 v3, v[24:25], v[28:29] offset0:32 offset1:40
	s_waitcnt vmcnt(48)
	v_cvt_pk_bf16_f32 v32, v32, v33
	v_cvt_pk_bf16_f32 v33, v34, v35
	v_cvt_pk_bf16_f32 v36, v36, v37
	v_cvt_pk_bf16_f32 v37, v38, v39
	ds_write2st64_b64 v3, v[32:33], v[36:37] offset0:48 offset1:56
	s_waitcnt lgkmcnt(0)
	s_barrier
	s_setprio 1
	s_mov_b32 m0, s26
	s_min_u32 s40, s25, 31
	s_bitcmp1_b32 s40, 4
	s_cselect_b32 s41, s23, s22
	s_lshl_b32 s42, s40, 23
	s_and_b32 s42, s42, 0x7000000
	s_or_b32 s41, s41, s42
	s_lshl_b32 s42, s40, 8
	s_and_b32 s42, s42, 0x100
	s_or_b32 s41, s41, s42
	s_sub_u32 s43, s25, 1
	s_min_u32 s43, s43, 31
	s_and_b32 s43, s43, 15
	s_lshl_b32 s43, s43, 15
	s_add_u32 s44, s43, s24
	v_mfma_f32_16x16x32_bf16 v[120:123], v[72:75], v[88:91], v[120:123]
	v_mfma_f32_16x16x32_bf16 v[124:127], v[76:79], v[88:91], v[124:127]
	buffer_load_dwordx4 v2, s[12:15], s44 offen sc1 lds
	v_mfma_f32_16x16x32_bf16 v[128:131], v[80:83], v[88:91], v[128:131]
	v_mfma_f32_16x16x32_bf16 v[132:135], v[84:87], v[88:91], v[132:135]
	buffer_load_dwordx4 v2, s[12:15], s44 offen offset:1024 sc1 lds
	v_mfma_f32_16x16x32_bf16 v[136:139], v[72:75], v[92:95], v[136:139]
	v_mfma_f32_16x16x32_bf16 v[140:143], v[76:79], v[92:95], v[140:143]
	buffer_load_dwordx4 v2, s[12:15], s44 offen offset:2048 sc1 lds
	v_mfma_f32_16x16x32_bf16 v[144:147], v[80:83], v[92:95], v[144:147]
	v_mfma_f32_16x16x32_bf16 v[148:151], v[84:87], v[92:95], v[148:151]
	buffer_load_dwordx4 v2, s[12:15], s44 offen offset:3072 sc1 lds
	v_mfma_f32_16x16x32_bf16 v[152:155], v[72:75], v[96:99], v[152:155]
	v_mfma_f32_16x16x32_bf16 v[156:159], v[76:79], v[96:99], v[156:159]
	v_mfma_f32_16x16x32_bf16 v[160:163], v[80:83], v[96:99], v[160:163]
	v_mfma_f32_16x16x32_bf16 v[164:167], v[84:87], v[96:99], v[164:167]
	buffer_load_dwordx4 v[8:11], v1, s[4:7], s41 offen sc0 nt
	v_mfma_f32_16x16x32_bf16 v[168:171], v[72:75], v[100:103], v[168:171]
	v_mfma_f32_16x16x32_bf16 v[172:175], v[76:79], v[100:103], v[172:175]
	v_mfma_f32_16x16x32_bf16 v[176:179], v[80:83], v[100:103], v[176:179]
	v_mfma_f32_16x16x32_bf16 v[180:183], v[84:87], v[100:103], v[180:183]
	s_add_u32 s42, s41, 0x4000
	buffer_load_dwordx4 v[12:15], v1, s[4:7], s42 offen sc0 nt
	v_mfma_f32_16x16x32_bf16 v[184:187], v[72:75], v[104:107], v[184:187]
	v_mfma_f32_16x16x32_bf16 v[188:191], v[76:79], v[104:107], v[188:191]
	v_mfma_f32_16x16x32_bf16 v[192:195], v[80:83], v[104:107], v[192:195]
	v_mfma_f32_16x16x32_bf16 v[196:199], v[84:87], v[104:107], v[196:199]
	s_add_u32 s42, s41, 0x8000
	buffer_load_dwordx4 v[16:19], v1, s[4:7], s42 offen sc0 nt
	v_mfma_f32_16x16x32_bf16 v[200:203], v[72:75], v[108:111], v[200:203]
	v_mfma_f32_16x16x32_bf16 v[204:207], v[76:79], v[108:111], v[204:207]
	v_mfma_f32_16x16x32_bf16 v[208:211], v[80:83], v[108:111], v[208:211]
	v_mfma_f32_16x16x32_bf16 v[212:215], v[84:87], v[108:111], v[212:215]
	s_add_u32 s42, s41, 0xc000
	buffer_load_dwordx4 v[20:23], v1, s[4:7], s42 offen sc0 nt
	v_mfma_f32_16x16x32_bf16 v[216:219], v[72:75], v[112:115], v[216:219]
	v_mfma_f32_16x16x32_bf16 v[220:223], v[76:79], v[112:115], v[220:223]
	v_mfma_f32_16x16x32_bf16 v[224:227], v[80:83], v[112:115], v[224:227]
	v_mfma_f32_16x16x32_bf16 v[228:231], v[84:87], v[112:115], v[228:231]
	v_mfma_f32_16x16x32_bf16 v[232:235], v[72:75], v[116:119], v[232:235]
	v_mfma_f32_16x16x32_bf16 v[236:239], v[76:79], v[116:119], v[236:239]
	v_mfma_f32_16x16x32_bf16 v[240:243], v[80:83], v[116:119], v[240:243]
	v_mfma_f32_16x16x32_bf16 v[244:247], v[84:87], v[116:119], v[244:247]
	s_add_u32 s26, s26, 0x8000
	s_cmp_eq_u32 s26, s32
	s_cselect_b32 s26, s27, s26
	s_setprio 0
	s_barrier
	ds_read_b128 v[72:75], v6 offset:1024
	ds_read_b128 v[76:79], v6 offset:3072
	ds_read_b128 v[80:83], v6 offset:5120
	ds_read_b128 v[84:87], v6 offset:7168
	ds_read_b128 v[88:91], v252 offset:33792
	ds_read_b128 v[92:95], v252 offset:35840
	ds_read_b128 v[96:99], v252 offset:37888
	ds_read_b128 v[100:103], v252 offset:39936
	ds_read_b128 v[104:107], v252 offset:41984
	ds_read_b128 v[108:111], v252 offset:44032
	ds_read_b128 v[112:115], v252 offset:46080
	ds_read_b128 v[116:119], v252 offset:48128
	s_waitcnt vmcnt(48)
	s_waitcnt lgkmcnt(0)
	s_barrier
	s_setprio 1
	s_add_u32 s33, s33, 0x8000
	s_cmp_eq_u32 s33, 0x18000
	s_cselect_b32 s33, 0, s33
	s_add_u32 s25, s25, 1
	v_mfma_f32_16x16x32_bf16 v[120:123], v[72:75], v[88:91], v[120:123]
	v_mfma_f32_16x16x32_bf16 v[124:127], v[76:79], v[88:91], v[124:127]
	v_mfma_f32_16x16x32_bf16 v[128:131], v[80:83], v[88:91], v[128:131]
	v_mfma_f32_16x16x32_bf16 v[132:135], v[84:87], v[88:91], v[132:135]
	s_add_u32 s42, s41, 0x10000
	buffer_load_dwordx4 v[24:27], v1, s[4:7], s42 offen sc0 nt
	v_mfma_f32_16x16x32_bf16 v[136:139], v[72:75], v[92:95], v[136:139]
	v_mfma_f32_16x16x32_bf16 v[140:143], v[76:79], v[92:95], v[140:143]
	v_mfma_f32_16x16x32_bf16 v[144:147], v[80:83], v[92:95], v[144:147]
	v_mfma_f32_16x16x32_bf16 v[148:151], v[84:87], v[92:95], v[148:151]
	v_mfma_f32_16x16x32_bf16 v[152:155], v[72:75], v[96:99], v[152:155]
	v_mfma_f32_16x16x32_bf16 v[156:159], v[76:79], v[96:99], v[156:159]
	v_mfma_f32_16x16x32_bf16 v[160:163], v[80:83], v[96:99], v[160:163]
	v_mfma_f32_16x16x32_bf16 v[164:167], v[84:87], v[96:99], v[164:167]
	s_add_u32 s42, s41, 0x14000
	buffer_load_dwordx4 v[28:31], v1, s[4:7], s42 offen sc0 nt
	v_mfma_f32_16x16x32_bf16 v[168:171], v[72:75], v[100:103], v[168:171]
	v_mfma_f32_16x16x32_bf16 v[172:175], v[76:79], v[100:103], v[172:175]
	v_mfma_f32_16x16x32_bf16 v[176:179], v[80:83], v[100:103], v[176:179]
	v_mfma_f32_16x16x32_bf16 v[180:183], v[84:87], v[100:103], v[180:183]
	v_mfma_f32_16x16x32_bf16 v[184:187], v[72:75], v[104:107], v[184:187]
	v_mfma_f32_16x16x32_bf16 v[188:191], v[76:79], v[104:107], v[188:191]
	v_mfma_f32_16x16x32_bf16 v[192:195], v[80:83], v[104:107], v[192:195]
	v_mfma_f32_16x16x32_bf16 v[196:199], v[84:87], v[104:107], v[196:199]
	s_add_u32 s42, s41, 0x18000
	buffer_load_dwordx4 v[32:35], v1, s[4:7], s42 offen sc0 nt
	v_mfma_f32_16x16x32_bf16 v[200:203], v[72:75], v[108:111], v[200:203]
	v_mfma_f32_16x16x32_bf16 v[204:207], v[76:79], v[108:111], v[204:207]
	v_mfma_f32_16x16x32_bf16 v[208:211], v[80:83], v[108:111], v[208:211]
	v_mfma_f32_16x16x32_bf16 v[212:215], v[84:87], v[108:111], v[212:215]
	v_mfma_f32_16x16x32_bf16 v[216:219], v[72:75], v[112:115], v[216:219]
	v_mfma_f32_16x16x32_bf16 v[220:223], v[76:79], v[112:115], v[220:223]
	v_mfma_f32_16x16x32_bf16 v[224:227], v[80:83], v[112:115], v[224:227]
	v_mfma_f32_16x16x32_bf16 v[228:231], v[84:87], v[112:115], v[228:231]
	s_add_u32 s42, s41, 0x1c000
	buffer_load_dwordx4 v[36:39], v1, s[4:7], s42 offen sc0 nt
	v_mfma_f32_16x16x32_bf16 v[232:235], v[72:75], v[116:119], v[232:235]
	v_mfma_f32_16x16x32_bf16 v[236:239], v[76:79], v[116:119], v[236:239]
	v_mfma_f32_16x16x32_bf16 v[240:243], v[80:83], v[116:119], v[240:243]
	v_mfma_f32_16x16x32_bf16 v[244:247], v[84:87], v[116:119], v[244:247]
	s_setprio 0
	s_barrier
	s_mov_b32 s39, 1
	s_mov_b32 s38, 7
	s_branch .Lg_loop
